# neighbourhood-attention unit loop: skip the vmcnt(0) + 32-register round-trip copy of the background-conversion buffer between two neighbourhood units
# baseline (speedup 1.0000x reference)
.LBB0_253:
	s_cmp_lt_i32 s30, 4
	s_cselect_b64 s[8:9], -1, 0
	s_and_b64 s[4:5], s[8:9], s[4:5]
	s_andn2_b64 vcc, exec, s[4:5]
	s_cbranch_vccnz .LBB0_364
	s_mov_b64 s[10:11], s[0:1]
	s_mov_b32 s98, 0
	s_load_dwordx2 s[4:5], s[10:11], 0xd8
	v_readlane_b32 s12, v255, 6
	s_mul_i32 s6, s12, 0x2080
	v_mbcnt_hi_u32_b32 v4, -1, v208
	s_add_i32 s6, s6, 0
	s_waitcnt lgkmcnt(0)
	s_add_u32 s23, s4, 0x11800000
	v_lshlrev_b32_e32 v2, 2, v4
	v_and_b32_e32 v210, 60, v2
	v_lshlrev_b32_e32 v2, 3, v4
	s_addc_u32 s26, s5, 0
	v_and_b32_e32 v194, 24, v2
	v_ashrrev_i32_e32 v211, 2, v4
	s_add_u32 s27, s4, 0x1800000
	v_ashrrev_i32_e32 v209, 4, v4
	s_movk_i32 s7, 0x104
	v_mul_u32_u24_e32 v2, 0x104, v194
	v_mov_b32_e32 v3, 0
	v_and_b32_e32 v5, -4, v4
	v_add_u32_e32 v213, 16, v211
	v_add_u32_e32 v215, 32, v211
	v_add_u32_e32 v217, 48, v211
	s_addc_u32 s35, s5, 0
	s_mov_b32 s65, 0
	v_lshl_add_u32 v220, v210, 2, s6
	v_mul_lo_u32 v221, v209, s7
	v_mov_b32_e32 v195, v3
	v_add3_u32 v219, s6, v2, v5
	v_ashrrev_i32_e32 v212, 31, v211
	v_ashrrev_i32_e32 v214, 31, v213
	v_ashrrev_i32_e32 v216, 31, v215
	s_cmpk_gt_i32 s88, 0x81f
	v_ashrrev_i32_e32 v218, 31, v217
	s_cbranch_scc1 .LBB0_352
	s_add_u32 s15, s4, 0x25b00000
	s_addc_u32 s48, s5, 0
	s_add_u32 s49, s4, 0x29c00000
	s_addc_u32 s50, s5, 0
	s_add_u32 s51, s4, 0x2dd00000
	s_addc_u32 s53, s5, 0
	v_and_b32_e32 v2, 31, v4
	v_ashrrev_i32_e32 v4, 3, v4
	s_lshl_b32 s54, s12, 5
	s_lshr_b32 s55, s3, 7
	v_and_b32_e32 v222, -4, v4
	v_lshl_add_u64 v[4:5], s[4:5], 0, v[2:3]
	s_mov_b64 s[4:5], 0x31e00000
	v_and_or_b32 v2, s54, 32, v2
	s_cmp_lg_u32 0, -1
	v_lshl_add_u64 v[196:197], v[4:5], 0, s[4:5]
	v_sub_u32_e64 v4, v2, 8 clamp
	s_cselect_b32 s4, 0, 0
	s_and_b32 s3, s3, 0xffffff80
	v_min_u32_e32 v223, 48, v4
	s_sub_i32 s3, s4, s3
	v_sub_u32_e32 v224, 15, v2
	v_add_u32_e32 v225, 16, v223
	s_mov_b32 s13, 0
	s_add_i32 s3, s3, 0x8800
	s_mov_b64 s[20:21], 0
	s_mov_b64 s[18:19], 0
	s_mov_b32 s56, 0x41000000
	s_mov_b32 s14, 0x42000000
	s_movk_i32 s57, 0x1e0
	s_movk_i32 s58, 0xffdf
	s_add_i32 s59, 0, 0x4000
	s_mov_b32 s60, s88
	s_mov_b32 s61, s88
	s_mov_b32 s63, 0
	s_mov_b32 s62, s52
	s_cmpk_gt_i32 s61, 0x7ff
	s_mov_b64 s[4:5], -1
	s_cbranch_scc0 .LBB0_290
	s_branch .LBB0_257
.LBB0_256:
	s_cmp_eq_u32 s98, 0
	s_cbranch_scc1 .Lnu_fullB
	s_mov_b32 s63, s65
	s_mov_b64 s[18:19], s[28:29]
	s_mov_b64 s[20:21], s[6:7]
	s_mov_b32 s62, s64
	s_branch .Lnu_doneB

.Lnu_doneB:
	s_cmpk_gt_i32 s61, 0x7ff
	s_mov_b64 s[4:5], -1
	s_cbranch_scc0 .LBB0_290

.LBB0_348:
	s_add_i32 s99, s61, s22
	s_cmpk_lt_i32 s99, 0x800
	s_cselect_b32 s98, 1, 0
	s_cbranch_scc0 .Lnu_fullA
	s_mov_b32 s65, s63
	s_mov_b64 s[28:29], s[18:19]
	s_mov_b64 s[6:7], s[20:21]
	s_mov_b32 s64, s62
	s_branch .Lnu_doneA

.Lnu_doneA:
	s_lshl_b32 s12, s44, 6
	v_cmp_gt_u32_e32 vcc, 32, v163
	s_and_saveexec_b64 s[4:5], vcc
	ds_write_b32 v164, v203 offset:32896
	s_or_b64 exec, exec, s[4:5]
	s_waitcnt lgkmcnt(0)
	v_lshl_add_u32 v2, v162, 4, s17
	ds_read_b128 v[36:39], v2 offset:32896
	ds_read_b128 v[40:43], v2 offset:32928
	s_mov_b64 s[38:39], s[12:13]
	ds_read_b128 v[44:47], v2 offset:32992
	s_waitcnt lgkmcnt(2)
	v_rcp_f32_e32 v50, v36
	v_rcp_f32_e32 v51, v37
	v_rcp_f32_e32 v52, v38
	v_rcp_f32_e32 v53, v39
	ds_read_b128 v[36:39], v2 offset:32960
	s_waitcnt lgkmcnt(2)
	v_rcp_f32_e32 v40, v40
	v_rcp_f32_e32 v41, v41
	v_rcp_f32_e32 v42, v42
	v_rcp_f32_e32 v43, v43
	s_waitcnt lgkmcnt(0)
	v_rcp_f32_e32 v36, v36
	v_rcp_f32_e32 v38, v38
	v_rcp_f32_e32 v44, v44
	v_rcp_f32_e32 v46, v46
	v_rcp_f32_e32 v47, v47
	v_rcp_f32_e32 v45, v45
	v_rcp_f32_e32 v39, v39
	v_rcp_f32_e32 v37, v37
	v_pk_mul_f32 v[34:35], v[34:35], v[46:47]
	v_pk_mul_f32 v[32:33], v[32:33], v[44:45]
	v_pk_mul_f32 v[30:31], v[30:31], v[38:39]
	v_pk_mul_f32 v[28:29], v[28:29], v[36:37]
	v_pk_mul_f32 v[26:27], v[26:27], v[42:43]
	v_pk_mul_f32 v[24:25], v[24:25], v[40:41]
	v_pk_mul_f32 v[22:23], v[22:23], v[52:53]
	v_pk_mul_f32 v[20:21], v[20:21], v[50:51]
	v_pk_mul_f32 v[48:49], v[18:19], v[46:47]
	v_pk_mul_f32 v[16:17], v[16:17], v[44:45]
	v_pk_mul_f32 v[14:15], v[14:15], v[38:39]
	v_pk_mul_f32 v[12:13], v[12:13], v[36:37]
	v_pk_mul_f32 v[10:11], v[10:11], v[42:43]
	v_pk_mul_f32 v[8:9], v[8:9], v[40:41]
	v_pk_mul_f32 v[6:7], v[6:7], v[52:53]
	v_pk_mul_f32 v[4:5], v[4:5], v[50:51]
	s_barrier
